# v21 plus quad K/V prefetch (7/2 split kept) plus LDS stash of the RG-LRU unit's conv weights and gate constants (ds_read instead of 26 global loads per unit)
# speedup vs baseline: 1.0056x; 1.0056x over previous
; __device__ __forceinline__ int fresh_lane() { int l; asm volatile("v_mbcnt_lo_u32_b32 %0, -1, 0\n\tv_mbcnt_hi_u32_b32 %0, -1, %0" : "=v"(l)); __builtin_assume(l >= 0 && l < 64); return l; }
; template <bool FINAL>
; __device__ __forceinline__ void lru_unit(const Args& a, unsigned char* lds_g, int b, int cidx, int blk, int tid, bf16x8_t (&wl)[2][2][4], int& wl_blk) {
;     const int lane = fresh_lane(), w = __builtin_amdgcn_readfirstlane(tid >> 6), fr = lane & 15, fq = lane >> 4; tid = w * 64 + lane;
;     float* zf = (float*)lds_g;
;     bf16* zb = (bf16*)(lds_g + 64 * 132 * 4);
;     const bool isctx = cidx < 4; const int seglen = isctx ? CTXL : SEQ, p0 = (isctx ? cidx : cidx - 4) * 64;
;     const bf16* UX = (const bf16*)(a.ws + WS_UX);
;     float gba[2], gbx[2], glam[2];
;     { const int ch_ = blk * 128 + 16 * w + fr;
; #pragma unroll
;       for (int d = 0; d < 2; ++d) { gba[d] = a.in[I_LBA][d * 1024 + ch_]; gbx[d] = a.in[I_LBX][d * 1024 + ch_]; glam[d] = a.in[I_LAM][d * 1024 + ch_]; } }
;     if (wl_blk != blk) { const bf16* WL = (const bf16*)(a.ws + WS_WL); wl_blk = blk;
; #pragma unroll
;       for (int d = 0; d < 2; ++d)
; #pragma unroll
;         for (int m = 0; m < 2; ++m)
; #pragma unroll
;             for (int ks = 0; ks < 4; ++ks) wl[d][m][ks] = *(const bf16x8_t*)(WL + ((size_t)((d * 2 + m) * 8 + blk) * 128 + 16 * w + fr) * 128 + 32 * ks + 8 * fq); }
;     __builtin_amdgcn_sched_barrier(0);
;     {
;         const int pos = tid >> 3, cg = tid & 7, ch0 = blk * 128 + cg * 16, p = p0 + pos;
;         float z[16];
; #pragma unroll
;         for (int q = 0; q < 4; ++q) { const f32x4 bv = *(const f32x4*)(a.in[I_CONVB] + ch0 + 4 * q); z[4 * q] = bv.x; z[4 * q + 1] = bv.y; z[4 * q + 2] = bv.z; z[4 * q + 3] = bv.w; }
;         v4u ua[4], ub[4]; float msk[4];
; #pragma unroll
;         for (int w4 = 0; w4 < 4; ++w4) { const int pp = p + w4 - 2; const bool ok = pp >= 0 && pp < seglen; const int ppc = ok ? pp : p;
;             const v4u* src = (const v4u*)(UX + (size_t)lru_pos_row(b, isctx, ppc) * 1024 + ch0); ua[w4] = src[0]; ub[w4] = src[1]; msk[w4] = ok ? 1.f : 0.f; }
.Lp2f_top:
	v_readfirstlane_b32 s1, v180
	v_mbcnt_lo_u32_b32 v189, -1, 0
	v_mbcnt_hi_u32_b32 v189, -1, v189
	s_lshl_b32 s0, s4, 7
	v_and_b32_e32 v188, 15, v189
	s_lshr_b32 s5, s1, 2
	s_and_b32 s5, s5, 0x3ffffff0
	v_or_b32_e32 v64, s0, v188
	v_add_u32_e32 v128, s5, v64
	v_lshlrev_b64 v[64:65], 2, v[128:129]
	v_lshl_add_u64 v[66:67], s[66:67], 0, v[64:65]
	v_add_lshl_u32 v193, v189, s1, 5
	v_add_u32_e32 v193, 0x12000, v193
	ds_read_b32 v135, v193 offset:0
	v_add_co_u32_e32 v66, vcc, s65, v66
	v_lshl_add_u64 v[68:69], s[70:71], 0, v[64:65]
	v_addc_co_u32_e32 v67, vcc, 0, v67, vcc
	ds_read_b32 v191, v193 offset:4
	v_add_co_u32_e32 v66, vcc, 0x1000, v68
	v_lshl_add_u64 v[64:65], s[16:17], 0, v[64:65]
	v_addc_co_u32_e32 v67, vcc, 0, v69, vcc
	ds_read_b32 v131, v193 offset:8
	v_add_co_u32_e32 v64, vcc, 0x1000, v64
	ds_read_b32 v134, v193 offset:12
	ds_read_b32 v192, v193 offset:16
	v_addc_co_u32_e32 v65, vcc, 0, v65, vcc
	ds_read_b32 v193, v193 offset:20
	v_or_b32_e32 v132, s5, v188
	v_lshrrev_b32_e32 v190, 4, v189
	v_add_u32_e32 v128, s0, v132
.LBB0_287_f:
	s_ashr_i32 s4, s41, 3
	s_mul_hi_i32 s5, s4, 0x38e38e39
	s_lshr_b32 s6, s5, 31
	s_ashr_i32 s25, s5, 3
	s_add_i32 s25, s25, s6
	s_mul_i32 s5, s25, 36
	s_sub_i32 s24, s4, s5
	s_andn2_b32 s1, s1, 63
	s_cmp_gt_i32 s24, 3
	s_cselect_b64 s[6:7], -1, 0
	s_lshl_b32 s43, s24, 6
	s_add_i32 s4, s43, 0xffffff00
	s_cmp_lt_i32 s24, 4
	v_or_b32_e32 v72, s1, v189
	s_cselect_b32 s44, s68, 0x800
	s_cselect_b32 s1, s43, s4
	v_lshlrev_b32_e32 v64, 4, v189
	v_and_b32_e32 v110, 0x70, v64
	v_or_b32_e32 v73, s0, v110
	v_lshlrev_b32_e32 v106, 2, v73
	v_and_b32_e32 v248, 7, v189
	v_mul_u32_u24_e32 v248, 0x140, v248
	v_add_u32_e32 v248, 0x10000, v248
	ds_read_b128 v[64:67], v248 offset:0
	ds_read_b128 v[68:71], v248 offset:16
	ds_read_b128 v[80:83], v248 offset:32
	ds_read_b128 v[92:95], v248 offset:48
	v_ashrrev_i32_e32 v111, 3, v72
	v_add_u32_e32 v112, s1, v111
	v_add_u32_e32 v72, -2, v112
	v_cmp_lt_i32_e32 vcc, 1, v112
	v_cmp_gt_i32_e64 s[4:5], s44, v72
	s_lshl_b32 s45, s25, 11
	s_and_b64 s[10:11], vcc, s[4:5]
	s_bitset1_b32 s45, 10
	v_cndmask_b32_e64 v74, v112, v72, s[10:11]
	s_mov_b64 s[0:1], -1
	s_and_b64 vcc, exec, s[6:7]
	s_cbranch_vccz .LBB0_289_f
	v_lshlrev_b32_e32 v72, 6, v74
	v_and_b32_e32 v72, 0x7c0, v72
	v_ashrrev_i32_e32 v75, 5, v74
	v_add3_u32 v72, v75, s45, v72
	s_mov_b64 s[0:1], 0

; template <bool FINAL>
; __device__ __forceinline__ void lru_unit(const Args& a, unsigned char* lds_g, int b, int cidx, int blk, int tid, bf16x8_t (&wl)[2][2][4], int& wl_blk) {
;     ...
;         for (int w4 = 0; w4 < 4; ++w4) { const int pp = p + w4 - 2; const bool ok = pp >= 0 && pp < seglen; const int ppc = ok ? pp : p;
;             const v4u* src = (const v4u*)(UX + (size_t)lru_pos_row(b, isctx, ppc) * 1024 + ch0); ua[w4] = src[0]; ub[w4] = src[1]; msk[w4] = ok ? 1.f : 0.f; }
; #pragma unroll
;         for (int w4 = 0; w4 < 4; ++w4) { const float* cw = a.in[I_CONVW] + w4 * 1024 + ch0;
;             const unsigned uu[8] = {ua[w4].x, ua[w4].y, ua[w4].z, ua[w4].w, ub[w4].x, ub[w4].y, ub[w4].z, ub[w4].w};
; #pragma unroll
;             for (int q = 0; q < 4; ++q) { const f32x4 cv = *(const f32x4*)(cw + 4 * q) * msk[w4]; z[4 * q] += cv.x * bflo(uu[2 * q]); z[4 * q + 1] += cv.y * bfhi(uu[2 * q]); z[4 * q + 2] += cv.z * bflo(uu[2 * q + 1]); z[4 * q + 3] += cv.w * bfhi(uu[2 * q + 1]); } }
.LBB0_303_f:
	v_mov_b32_e32 v107, v129
	v_lshl_add_u64 v[126:127], s[60:61], 0, v[106:107]
	v_add_co_u32_e32 v152, vcc, s69, v126
	ds_read_b128 v[114:117], v248 offset:64
	ds_read_b128 v[118:121], v248 offset:80
	v_addc_co_u32_e32 v153, vcc, 0, v127, vcc
	ds_read_b128 v[122:125], v248 offset:96
	ds_read_b128 v[136:139], v248 offset:112
	ds_read_b128 v[140:143], v248 offset:128
	v_lshl_add_u64 v[106:107], v[126:127], 0, s[50:51]
	v_ashrrev_i32_e32 v109, 31, v108
	ds_read_b128 v[144:147], v248 offset:144
	ds_read_b128 v[148:151], v248 offset:160
	v_lshlrev_b64 v[172:173], 11, v[108:109]
	ds_read_b128 v[106:109], v248 offset:176
	v_lshl_add_u64 v[164:165], v[126:127], 0, s[54:55]
	ds_read_b128 v[152:155], v248 offset:192
	s_nop 0
	ds_read_b128 v[156:159], v248 offset:208
	ds_read_b128 v[160:163], v248 offset:224
	s_nop 0
	ds_read_b128 v[164:167], v248 offset:240
	v_lshl_add_u64 v[104:105], v[104:105], 0, v[172:173]
	v_add_co_u32_e32 v168, vcc, s72, v126
	s_nop 0
	v_addc_co_u32_e32 v169, vcc, 0, v127, vcc
	v_lshl_add_u64 v[126:127], v[126:127], 0, s[56:57]
	ds_read_b128 v[168:171], v248 offset:256
	s_nop 0
	ds_read_b128 v[176:179], v248 offset:272
	ds_read_b128 v[198:201], v248 offset:288
	ds_read_b128 v[202:205], v248 offset:304
	v_cndmask_b32_e64 v206, 0, 1.0, s[10:11]
	v_cmp_gt_u32_e32 vcc, s44, v112
	v_cndmask_b32_e64 v112, 0, 1.0, s[4:5]
	s_waitcnt vmcnt(0) lgkmcnt(0)
	s_branch .Lp2_join

; __device__ __forceinline__ int fresh_lane() { int l; asm volatile("v_mbcnt_lo_u32_b32 %0, -1, 0\n\tv_mbcnt_hi_u32_b32 %0, -1, %0" : "=v"(l)); __builtin_assume(l >= 0 && l < 64); return l; }
; template <bool FINAL>
; __device__ __forceinline__ void lru_unit(const Args& a, unsigned char* lds_g, int b, int cidx, int blk, int tid, bf16x8_t (&wl)[2][2][4], int& wl_blk) {
;     const int lane = fresh_lane(), w = __builtin_amdgcn_readfirstlane(tid >> 6), fr = lane & 15, fq = lane >> 4; tid = w * 64 + lane;
;     float* zf = (float*)lds_g;
;     bf16* zb = (bf16*)(lds_g + 64 * 132 * 4);
;     const bool isctx = cidx < 4; const int seglen = isctx ? CTXL : SEQ, p0 = (isctx ? cidx : cidx - 4) * 64;
;     const bf16* UX = (const bf16*)(a.ws + WS_UX);
;     float gba[2], gbx[2], glam[2];
;     { const int ch_ = blk * 128 + 16 * w + fr;
; #pragma unroll
;       for (int d = 0; d < 2; ++d) { gba[d] = a.in[I_LBA][d * 1024 + ch_]; gbx[d] = a.in[I_LBX][d * 1024 + ch_]; glam[d] = a.in[I_LAM][d * 1024 + ch_]; } }
;     if (wl_blk != blk) { const bf16* WL = (const bf16*)(a.ws + WS_WL); wl_blk = blk;
; #pragma unroll
;       for (int d = 0; d < 2; ++d)
; #pragma unroll
;         for (int m = 0; m < 2; ++m)
; #pragma unroll
;             for (int ks = 0; ks < 4; ++ks) wl[d][m][ks] = *(const bf16x8_t*)(WL + ((size_t)((d * 2 + m) * 8 + blk) * 128 + 16 * w + fr) * 128 + 32 * ks + 8 * fq); }
.LBB0_285:
	s_and_b32 s4, s41, 7
	s_cmp_eq_u32 s42, s4
	s_cbranch_scc1 .Lp2f_top
	v_readfirstlane_b32 s1, v180
	v_mbcnt_lo_u32_b32 v189, -1, 0
	v_mbcnt_hi_u32_b32 v189, -1, v189
	s_lshl_b32 s0, s4, 7
	v_and_b32_e32 v188, 15, v189
	s_lshr_b32 s5, s1, 2
	s_and_b32 s5, s5, 0x3ffffff0
	v_or_b32_e32 v64, s0, v188
	v_add_u32_e32 v128, s5, v64
	v_lshlrev_b64 v[64:65], 2, v[128:129]
	s_load_dwordx16 s[16:31], s[96:97], 0x80
	v_lshl_add_u64 v[66:67], s[66:67], 0, v[64:65]
	global_load_dword v135, v[66:67], off
	v_add_co_u32_e32 v66, vcc, s65, v66
	s_waitcnt lgkmcnt(0)
	v_lshl_add_u64 v[68:69], s[70:71], 0, v[64:65]
	v_addc_co_u32_e32 v67, vcc, 0, v67, vcc
	global_load_dword v191, v[66:67], off
	v_add_co_u32_e32 v66, vcc, 0x1000, v68
	s_waitcnt lgkmcnt(0)
	v_lshl_add_u64 v[64:65], s[16:17], 0, v[64:65]
	v_addc_co_u32_e32 v67, vcc, 0, v69, vcc
	global_load_dword v131, v[64:65], off
	v_add_co_u32_e32 v64, vcc, 0x1000, v64
	global_load_dword v134, v[68:69], off
	global_load_dword v192, v[66:67], off
	v_addc_co_u32_e32 v65, vcc, 0, v65, vcc
	global_load_dword v193, v[64:65], off
	v_or_b32_e32 v132, s5, v188
	v_lshrrev_b32_e32 v190, 4, v189
	s_cmp_eq_u32 s42, s4
	v_add_u32_e32 v128, s0, v132
	s_cbranch_scc1 .LBB0_287
	v_lshlrev_b32_e32 v0, 4, v190
	v_mov_b32_e32 v1, v129
	v_add_u32_e32 v16, 0x400, v128
	v_mov_b32_e32 v17, v129
	v_add_u32_e32 v32, 0x800, v128
	v_mov_b32_e32 v33, v129
	v_add_u32_e32 v50, 0xc00, v128
	v_mov_b32_e32 v51, v129
	v_lshl_add_u64 v[48:49], s[48:49], 0, v[0:1]
	v_lshlrev_b64 v[0:1], 8, v[128:129]
	v_lshlrev_b64 v[16:17], 8, v[16:17]
	v_lshlrev_b64 v[32:33], 8, v[32:33]
	v_lshlrev_b64 v[50:51], 8, v[50:51]
	v_lshl_add_u64 v[12:13], v[48:49], 0, v[0:1]
	v_lshl_add_u64 v[28:29], v[48:49], 0, v[16:17]
	v_lshl_add_u64 v[44:45], v[48:49], 0, v[32:33]
	v_lshl_add_u64 v[60:61], v[48:49], 0, v[50:51]
	global_load_dwordx4 v[0:3], v[12:13], off
	global_load_dwordx4 v[4:7], v[12:13], off offset:64
	global_load_dwordx4 v[8:11], v[12:13], off offset:128
	s_nop 0
	global_load_dwordx4 v[12:15], v[12:13], off offset:192
	s_nop 0
	global_load_dwordx4 v[16:19], v[28:29], off
	global_load_dwordx4 v[20:23], v[28:29], off offset:64
	global_load_dwordx4 v[24:27], v[28:29], off offset:128
	s_nop 0
	global_load_dwordx4 v[28:31], v[28:29], off offset:192
	s_nop 0
	global_load_dwordx4 v[32:35], v[44:45], off
	global_load_dwordx4 v[36:39], v[44:45], off offset:64
	global_load_dwordx4 v[40:43], v[44:45], off offset:128
	s_nop 0
	global_load_dwordx4 v[44:47], v[44:45], off offset:192
	s_nop 0
	global_load_dwordx4 v[48:51], v[60:61], off
	global_load_dwordx4 v[52:55], v[60:61], off offset:64
	global_load_dwordx4 v[56:59], v[60:61], off offset:128
	s_nop 0
	global_load_dwordx4 v[60:63], v[60:61], off offset:192
	s_mov_b32 s42, s4

; template <bool FINAL>
; __device__ __forceinline__ void lru_unit(const Args& a, unsigned char* lds_g, int b, int cidx, int blk, int tid, bf16x8_t (&wl)[2][2][4], int& wl_blk) {
;     ...
;         const int pos = tid >> 3, cg = tid & 7, ch0 = blk * 128 + cg * 16, p = p0 + pos;
;         float z[16];
; #pragma unroll
;         for (int q = 0; q < 4; ++q) { const f32x4 bv = *(const f32x4*)(a.in[I_CONVB] + ch0 + 4 * q); z[4 * q] = bv.x; z[4 * q + 1] = bv.y; z[4 * q + 2] = bv.z; z[4 * q + 3] = bv.w; }
;         v4u ua[4], ub[4]; float msk[4];
; #pragma unroll
;         for (int w4 = 0; w4 < 4; ++w4) { const int pp = p + w4 - 2; const bool ok = pp >= 0 && pp < seglen; const int ppc = ok ? pp : p;
;             const v4u* src = (const v4u*)(UX + (size_t)lru_pos_row(b, isctx, ppc) * 1024 + ch0); ua[w4] = src[0]; ub[w4] = src[1]; msk[w4] = ok ? 1.f : 0.f; }
; #pragma unroll
;         for (int w4 = 0; w4 < 4; ++w4) { const float* cw = a.in[I_CONVW] + w4 * 1024 + ch0;
;             const unsigned uu[8] = {ua[w4].x, ua[w4].y, ua[w4].z, ua[w4].w, ub[w4].x, ub[w4].y, ub[w4].z, ub[w4].w};
; #pragma unroll
;             for (int q = 0; q < 4; ++q) { const f32x4 cv = *(const f32x4*)(cw + 4 * q) * msk[w4]; z[4 * q] += cv.x * bflo(uu[2 * q]); z[4 * q + 1] += cv.y * bfhi(uu[2 * q]); z[4 * q + 2] += cv.z * bflo(uu[2 * q + 1]); z[4 * q + 3] += cv.w * bfhi(uu[2 * q + 1]); } }
.LBB0_303:
	v_mov_b32_e32 v107, v129
	v_lshl_add_u64 v[126:127], s[60:61], 0, v[106:107]
	v_add_co_u32_e32 v152, vcc, s69, v126
	global_load_dwordx4 v[114:117], v106, s[60:61]
	global_load_dwordx4 v[118:121], v106, s[60:61] offset:16
	v_addc_co_u32_e32 v153, vcc, 0, v127, vcc
	global_load_dwordx4 v[122:125], v106, s[60:61] offset:48
	global_load_dwordx4 v[136:139], v106, s[60:61] offset:32
	global_load_dwordx4 v[140:143], v[152:153], off offset:-4096
	v_lshl_add_u64 v[106:107], v[126:127], 0, s[50:51]
	v_ashrrev_i32_e32 v109, 31, v108
	global_load_dwordx4 v[144:147], v[106:107], off offset:16
	global_load_dwordx4 v[148:151], v[106:107], off offset:32
	v_lshlrev_b64 v[172:173], 11, v[108:109]
	global_load_dwordx4 v[106:109], v[106:107], off offset:48
	v_lshl_add_u64 v[164:165], v[126:127], 0, s[54:55]
	global_load_dwordx4 v[152:155], v[152:153], off
	s_nop 0
	global_load_dwordx4 v[156:159], v[164:165], off offset:16
	global_load_dwordx4 v[160:163], v[164:165], off offset:48
	s_nop 0
	global_load_dwordx4 v[164:167], v[164:165], off offset:32
	v_lshl_add_u64 v[104:105], v[104:105], 0, v[172:173]
	v_add_co_u32_e32 v168, vcc, s72, v126
	s_nop 0
	v_addc_co_u32_e32 v169, vcc, 0, v127, vcc
	v_lshl_add_u64 v[126:127], v[126:127], 0, s[56:57]
	global_load_dwordx4 v[168:171], v[168:169], off
	s_nop 0
	global_load_dwordx4 v[176:179], v[126:127], off offset:16
	global_load_dwordx4 v[198:201], v[126:127], off offset:32
	global_load_dwordx4 v[202:205], v[126:127], off offset:48
	v_cndmask_b32_e64 v206, 0, 1.0, s[10:11]
	v_cmp_gt_u32_e32 vcc, s44, v112
	v_cndmask_b32_e64 v112, 0, 1.0, s[4:5]
	s_waitcnt vmcnt(0)
	v_readfirstlane_b32 s81, v180
	s_andn2_b32 s81, s81, 63
	v_mbcnt_lo_u32_b32 v248, -1, 0
	v_mbcnt_hi_u32_b32 v248, -1, v248
	v_add_lshl_u32 v248, v248, s81, 5
	v_add_u32_e32 v248, 0x12000, v248
	ds_write_b32 v248, v135
	ds_write_b32 v248, v191 offset:4
	ds_write_b32 v248, v131 offset:8
	ds_write_b32 v248, v134 offset:12
	ds_write_b32 v248, v192 offset:16
	ds_write_b32 v248, v193 offset:20
	v_mbcnt_lo_u32_b32 v248, -1, 0
	v_mbcnt_hi_u32_b32 v248, -1, v248
	v_and_b32_e32 v248, 7, v248
	v_mul_u32_u24_e32 v248, 0x140, v248
	v_add_u32_e32 v248, 0x10000, v248
	ds_write_b128 v248, v[64:67]
	ds_write_b128 v248, v[68:71] offset:16
	ds_write_b128 v248, v[80:83] offset:32
	ds_write_b128 v248, v[92:95] offset:48
	ds_write_b128 v248, v[114:117] offset:64
	ds_write_b128 v248, v[118:121] offset:80
	ds_write_b128 v248, v[122:125] offset:96
	ds_write_b128 v248, v[136:139] offset:112
	ds_write_b128 v248, v[140:143] offset:128
	ds_write_b128 v248, v[144:147] offset:144
	ds_write_b128 v248, v[148:151] offset:160
	ds_write_b128 v248, v[106:109] offset:176
	ds_write_b128 v248, v[152:155] offset:192
	ds_write_b128 v248, v[156:159] offset:208
	ds_write_b128 v248, v[160:163] offset:224
	ds_write_b128 v248, v[164:167] offset:240
	ds_write_b128 v248, v[168:171] offset:256
	ds_write_b128 v248, v[176:179] offset:272
	ds_write_b128 v248, v[198:201] offset:288
	ds_write_b128 v248, v[202:205] offset:304
.Lp2_join:
	v_mov_b64_e32 v[88:89], v[220:221]
	v_mov_b64_e32 v[90:91], v[222:223]
	v_mov_b64_e32 v[72:73], v[216:217]
	v_mov_b64_e32 v[74:75], v[218:219]
	v_mov_b64_e32 v[96:97], v[228:229]
	v_mov_b64_e32 v[98:99], v[230:231]
	v_mov_b64_e32 v[76:77], v[224:225]
	v_mov_b64_e32 v[78:79], v[226:227]
	v_mov_b64_e32 v[100:101], v[236:237]
	v_mov_b64_e32 v[102:103], v[238:239]
	v_mov_b64_e32 v[84:85], v[232:233]
	v_mov_b64_e32 v[86:87], v[234:235]
	v_mov_b64_e32 v[172:173], v[244:245]
	v_mov_b64_e32 v[174:175], v[246:247]
	v_mov_b64_e32 v[194:195], v[240:241]
	v_mov_b64_e32 v[196:197], v[242:243]
	s_add_i32 s73, s41, s101
	s_cmp_lt_i32 s73, s100
	s_cbranch_scc0 .Lp2pf_skip
	s_and_b32 s74, s73, 7
	s_lshl_b32 s74, s74, 8
	s_ashr_i32 s75, s73, 3
	s_mul_hi_i32 s76, s75, 0x38e38e39
	s_ashr_i32 s76, s76, 3
	s_mul_i32 s77, s76, 36
	s_sub_i32 s77, s75, s77
	s_lshl_b32 s78, s77, 6
	s_add_i32 s79, s78, 0xffffff00
	s_lshl_b32 s80, s76, 8
	s_lshl_b32 s81, s76, 11
	s_bitset1_b32 s81, 10
	s_cmp_lt_i32 s77, 4
	s_cselect_b32 s78, s78, s79
	s_movk_i32 s79, 0x800
	s_cselect_b32 s79, 0x100, s79
	s_cselect_b32 s80, s80, s81
	s_cselect_b64 s[88:89], -1, 0
	v_mbcnt_lo_u32_b32 v248, -1, 0
	v_mbcnt_hi_u32_b32 v248, -1, v248
	v_readfirstlane_b32 s81, v180
	s_andn2_b32 s81, s81, 63
	v_or_b32_e32 v216, s81, v248
	v_lshrrev_b32_e32 v216, 3, v216
	v_add_u32_e32 v216, s78, v216
	v_and_b32_e32 v217, 7, v248
	v_lshl_or_b32 v217, v217, 5, s74
	v_add_u32_e32 v220, -2, v216
	v_cmp_gt_u32_e64 s[90:91], s79, v220
	v_cndmask_b32_e64 v220, v216, v220, s[90:91]
	v_and_b32_e32 v218, 31, v220
	v_lshrrev_b32_e32 v219, 5, v220
	v_lshl_or_b32 v218, v218, 6, v219
	v_cndmask_b32_e64 v220, v218, v220, s[88:89]
	v_add_lshl_u32 v220, v220, s80, 11
	v_or_b32_e32 v220, v220, v217
	v_mov_b32_e32 v221, 0
	v_add_u32_e32 v228, -1, v216
	v_cmp_gt_u32_e64 s[90:91], s79, v228
	v_cndmask_b32_e64 v228, v216, v228, s[90:91]
	v_and_b32_e32 v218, 31, v228
	v_lshrrev_b32_e32 v219, 5, v228
	v_lshl_or_b32 v218, v218, 6, v219
	v_cndmask_b32_e64 v228, v218, v228, s[88:89]
	v_add_lshl_u32 v228, v228, s80, 11
	v_or_b32_e32 v228, v228, v217
	v_mov_b32_e32 v229, 0
	v_mov_b32_e32 v236, v216
	v_and_b32_e32 v218, 31, v236
	v_lshrrev_b32_e32 v219, 5, v236
	v_lshl_or_b32 v218, v218, 6, v219
	v_cndmask_b32_e64 v236, v218, v236, s[88:89]
	v_add_lshl_u32 v236, v236, s80, 11
	v_or_b32_e32 v236, v236, v217
	v_mov_b32_e32 v237, 0
	v_add_u32_e32 v244, 1, v216
	v_cmp_gt_u32_e64 s[90:91], s79, v244
	v_cndmask_b32_e64 v244, v216, v244, s[90:91]
	v_and_b32_e32 v218, 31, v244
	v_lshrrev_b32_e32 v219, 5, v244
	v_lshl_or_b32 v218, v218, 6, v219
	v_cndmask_b32_e64 v244, v218, v244, s[88:89]
	v_add_lshl_u32 v244, v244, s80, 11
	v_or_b32_e32 v244, v244, v217
	v_mov_b32_e32 v245, 0
	v_lshl_add_u64 v[220:221], v[220:221], 0, s[14:15]
	v_lshl_add_u64 v[228:229], v[228:229], 0, s[14:15]
	v_lshl_add_u64 v[236:237], v[236:237], 0, s[14:15]
	v_lshl_add_u64 v[244:245], v[244:245], 0, s[14:15]
	global_load_dwordx4 v[216:219], v[220:221], off offset:16
	s_nop 0
	global_load_dwordx4 v[220:223], v[220:221], off
	s_nop 0
	global_load_dwordx4 v[224:227], v[228:229], off offset:16
	s_nop 0
	global_load_dwordx4 v[228:231], v[228:229], off
	s_nop 0
	global_load_dwordx4 v[232:235], v[236:237], off offset:16
	s_nop 0
	global_load_dwordx4 v[236:239], v[236:237], off
	s_nop 0
	global_load_dwordx4 v[240:243], v[244:245], off offset:16
	s_nop 0
	global_load_dwordx4 v[244:247], v[244:245], off
	s_nop 0
